# MLA-hosted conversion: real slice loads every other key tile (two tiles of latency), 3 tasks per wave = last 6144 down tasks; drain stops at 18432
# speedup vs baseline: 1.0050x; 1.0009x over previous
.LBB0_570:
	s_waitcnt lgkmcnt(4)
	v_mfma_scale_f32_32x32x64_f8f6f4 v[80:95], v[80:87], v[120:127], 0, v205, v205 op_sel_hi:[0,0,0]
	s_mov_b64 s[4:5], exec
	s_cmp_ge_u32 s18, s20
	s_waitcnt lgkmcnt(2)
	v_mfma_scale_f32_32x32x64_f8f6f4 v[80:95], v[104:111], v[128:135], v[80:95], v205, v205 op_sel_hi:[0,0,0]
	s_waitcnt lgkmcnt(0)
	v_mfma_scale_f32_32x32x64_f8f6f4 v[80:95], v[96:103], v[136:143], v[80:95], v205, v205 op_sel_hi:[0,0,0]
	s_nop 15
	s_nop 3
	v_max_f32_e32 v96, v80, v81
	v_max3_f32 v96, v96, v82, v83
	v_max3_f32 v96, v96, v84, v85
	v_max3_f32 v96, v96, v86, v87
	v_max3_f32 v96, v96, v88, v89
	v_max3_f32 v96, v96, v90, v91
	v_max3_f32 v96, v96, v92, v93
	v_max3_f32 v96, v96, v94, v95
	v_mov_b32_e32 v97, v96
	s_nop 1
	v_permlane32_swap_b32_e32 v96, v97
	v_max_f32_e32 v96, v96, v97
	v_fma_f32 v97, v96, s40, -v192
	v_cmp_ge_f32_e32 vcc, s70, v97
	s_cbranch_scc1 .LBB0_577
	s_xor_b32 s25, s23, 1
	s_lshl_b32 s18, s25, 15
	s_add_i32 s26, s18, 0
	v_add3_u32 v97, s26, v212, v190
	s_waitcnt vmcnt(3)
	ds_write_b128 v97, v[168:171]
	s_and_saveexec_b64 s[18:19], s[0:1]
	v_add3_u32 v97, s26, v215, v188
	ds_write_b128 v97, v[164:167]
	s_or_b64 exec, exec, s[18:19]
	v_lshl_add_u32 v97, s25, 14, v207
	s_cmp_ge_u32 s78, s74
	s_waitcnt vmcnt(2)
	ds_write_b128 v97, v[172:175]
	s_bitcmp1_b32 s98, 0
	s_cbranch_scc1 .Lcv_done_0
	s_cmp_gt_u32 s98, 53
	s_cbranch_scc1 .Lcv_done_0
	s_waitcnt vmcnt(0)
	s_lshr_b32 s26, s98, 1
	s_mul_i32 s18, s26, 57
	s_lshr_b32 s18, s18, 9
	s_mul_i32 s19, s18, 9
	s_sub_i32 s19, s26, s19
	s_cmp_eq_u32 s19, 0
	s_cbranch_scc1 .Lcv_setup_0
	v_mul_f32_e32 v244, 0x42000000, v244
	v_mul_f32_e32 v245, 0x42000000, v245
	v_mul_f32_e32 v246, 0x42000000, v246
	v_mul_f32_e32 v247, 0x42000000, v247
	v_mul_f32_e32 v248, 0x42000000, v248
	v_mul_f32_e32 v249, 0x42000000, v249
	v_mul_f32_e32 v250, 0x42000000, v250
	v_mul_f32_e32 v251, 0x42000000, v251
	v_med3_f32 v244, v244, s69, v203
	v_med3_f32 v245, v245, s69, v203
	v_med3_f32 v246, v246, s69, v203
	v_med3_f32 v247, v247, s69, v203
	v_med3_f32 v248, v248, s69, v203
	v_med3_f32 v249, v249, s69, v203
	v_med3_f32 v250, v250, s69, v203
	v_med3_f32 v251, v251, s69, v203
	v_cvt_pk_fp8_f32 v244, v244, v248
	v_cvt_pk_fp8_f32 v245, v245, v249
	v_cvt_pk_fp8_f32 v246, v246, v250
	v_cvt_pk_fp8_f32 v247, v247, v251
	s_nop 0
	ds_write_b16 v243, v244
	ds_write_b16 v243, v245 offset:80
	ds_write_b16 v243, v246 offset:160
	ds_write_b16 v243, v247 offset:240
	v_add_u32_e32 v243, 2, v243
	s_cmp_eq_u32 s19, 8
	s_cbranch_scc1 .Lcv_store_0
	s_add_u32 s100, s100, 0x4000
	s_addc_u32 s101, s101, 0
	s_branch .Lcv_next_0
.Lcv_setup_0:
	s_lshl_b32 s25, s14, 3
	s_add_i32 s25, s25, s82
	s_lshr_b32 s26, s25, 8
	s_lshl_b32 s27, s18, 3
	s_add_i32 s26, s26, s27
	s_add_i32 s26, s26, 8
	s_and_b32 s25, s25, 255
	v_mov_b32_e32 v223, 0x204f8
	ds_read_b64 v[244:245], v223
	s_and_b32 s27, s25, 7
	s_lshl_b32 s27, s27, 19
	s_lshr_b32 s19, s25, 3
	s_lshl_b32 s19, s19, 8
	s_add_i32 s27, s27, s19
	s_lshl_b32 s26, s26, 22
	s_add_i32 s26, s26, s27
	s_waitcnt lgkmcnt(0)
	v_readfirstlane_b32 s100, v244
	v_readfirstlane_b32 s101, v245
	v_bfe_u32 v243, v241, 4, 4
	v_mul_u32_u24_e32 v243, 0x140, v243
	v_lshrrev_b32_e32 v223, 17, v241
	v_lshl_add_u32 v243, v223, 4, v243
	v_add_u32_e32 v243, s99, v243
	s_add_u32 s100, s100, s26
	s_addc_u32 s101, s101, 0
	s_branch .Lcv_next_0
.Lcv_store_0:
	s_lshl_b32 s25, s14, 3
	s_add_i32 s25, s25, s82
	s_lshr_b32 s26, s25, 8
	s_lshl_b32 s27, s18, 3
	s_add_i32 s26, s26, s27
	s_add_i32 s26, s26, 8
	s_and_b32 s25, s25, 255
	s_and_b32 s27, s25, 7
	s_lshl_b32 s27, s27, 6
	s_lshr_b32 s19, s25, 3
	s_lshl_b32 s19, s19, 15
	s_add_i32 s27, s27, s19
	s_lshl_b32 s26, s26, 20
	s_add_i32 s25, s27, s26
	s_add_u32 s26, s34, 0x17458000
	s_addc_u32 s27, s35, 0
	s_add_u32 s26, s26, s25
	s_addc_u32 s27, s27, 0
	v_mbcnt_hi_u32_b32 v252, -1, v253
	v_lshrrev_b32_e32 v223, 2, v252
	v_and_b32_e32 v252, 3, v252
	v_lshlrev_b32_e32 v252, 4, v252
	v_mul_u32_u24_e32 v244, 0x50, v223
	v_lshl_add_u32 v223, v223, 9, v252
	v_add3_u32 v252, v244, v252, s99
	s_waitcnt lgkmcnt(0)
	ds_read_b128 v[244:247], v252
	ds_read_b128 v[248:251], v252 offset:1280
	s_waitcnt lgkmcnt(0)
	global_store_dwordx4 v223, v[244:247], s[26:27]
	s_add_u32 s26, s26, 0x2000
	s_addc_u32 s27, s27, 0
	s_nop 0
	global_store_dwordx4 v223, v[248:251], s[26:27]
	s_add_u32 s26, s26, 0x2000
	s_addc_u32 s27, s27, 0
	ds_read_b128 v[244:247], v252 offset:2560
	ds_read_b128 v[248:251], v252 offset:3840
	s_waitcnt lgkmcnt(0)
	global_store_dwordx4 v223, v[244:247], s[26:27]
	s_add_u32 s26, s26, 0x2000
	s_addc_u32 s27, s27, 0
	s_nop 0
	global_store_dwordx4 v223, v[248:251], s[26:27]
.Lcv_next_0:
.Lcv_done_0:
	s_add_i32 s98, s98, 1
	s_cmp_ge_u32 s78, s74
	s_cbranch_scc1 .LBB0_577
	s_cmp_lt_u32 s78, s77
	s_cselect_b32 s18, 0, s77
	s_cselect_b32 s19, s76, s75
	s_lshl_b32 s18, s18, 6
	s_sub_i32 s25, s19, s18
	s_add_i32 s25, s25, s22
	v_add_u32_e32 v97, s25, v210
	v_mad_i64_i32 v[98:99], s[18:19], v97, s64, v[194:195]
	global_load_dwordx4 v[168:171], v[98:99], off
	s_and_saveexec_b64 s[18:19], s[0:1]
	s_cbranch_execz .LBB0_576
	v_add_u32_e32 v97, s25, v213
	v_mad_i64_i32 v[98:99], s[26:27], v97, s64, v[196:197]
	global_load_dwordx4 v[164:167], v[98:99], off
.LBB0_576:
	s_or_b64 exec, exec, s[18:19]
	s_ashr_i32 s18, s25, 6
	s_ashr_i32 s19, s18, 31
	s_lshl_b64 s[18:19], s[18:19], 16
	v_lshl_add_u64 v[98:99], v[198:199], 0, s[18:19]
	global_load_dwordx4 v[172:175], v[98:99], off
	s_bitcmp1_b32 s98, 0
	s_cbranch_scc0 .Lcv_dummy_0
	global_load_dwordx4 v[244:247], v241, s[100:101] nt
	global_load_dwordx4 v[248:251], v242, s[100:101] nt
	s_branch .LBB0_577
.Lcv_dummy_0:
	global_load_dword v252, v241, s[100:101]
	global_load_dword v252, v241, s[100:101]

.LBB0_580:
	s_waitcnt vmcnt(0)
	ds_read_b128 v[80:83], v216 offset:39424
	ds_read_b128 v[84:87], v216 offset:39440
	ds_read_b128 v[104:107], v216 offset:39488
	ds_read_b128 v[108:111], v216 offset:39504
	v_add_u32_e32 v89, v216, v217
	ds_read_b128 v[96:99], v89 offset:39552
	ds_read_b128 v[100:103], v89 offset:39584
	v_cmp_gt_f32_e32 vcc, 1.0, v88
	s_cbranch_vccz .LBB0_584
	s_and_saveexec_b64 s[4:5], s[2:3]
	ds_write_b32 v209, v88 offset:128
	s_or_b64 exec, exec, s[4:5]
	s_waitcnt lgkmcnt(0)
	ds_read_b128 v[88:91], v214 offset:224
	ds_read_b128 v[92:95], v214 offset:192
	ds_read_b128 v[144:147], v214 offset:160
	ds_read_b128 v[148:151], v214 offset:128
	s_waitcnt lgkmcnt(3)
	v_pk_mul_f32 v[62:63], v[62:63], v[90:91]
	s_waitcnt lgkmcnt(2)
	v_pk_mul_f32 v[58:59], v[58:59], v[94:95]
	s_waitcnt lgkmcnt(1)
	v_pk_mul_f32 v[54:55], v[54:55], v[146:147]
	s_waitcnt lgkmcnt(0)
	v_pk_mul_f32 v[50:51], v[50:51], v[150:151]
	v_pk_mul_f32 v[60:61], v[60:61], v[88:89]
	v_pk_mul_f32 v[56:57], v[56:57], v[92:93]
	v_pk_mul_f32 v[52:53], v[52:53], v[144:145]
	v_pk_mul_f32 v[48:49], v[48:49], v[148:149]
	v_pk_mul_f32 v[46:47], v[46:47], v[90:91]
	v_pk_mul_f32 v[42:43], v[42:43], v[94:95]
	v_pk_mul_f32 v[38:39], v[38:39], v[146:147]
	v_pk_mul_f32 v[34:35], v[34:35], v[150:151]
	v_pk_mul_f32 v[44:45], v[44:45], v[88:89]
	v_pk_mul_f32 v[40:41], v[40:41], v[92:93]
	v_pk_mul_f32 v[36:37], v[36:37], v[144:145]
	v_pk_mul_f32 v[32:33], v[32:33], v[148:149]
	v_pk_mul_f32 v[30:31], v[30:31], v[90:91]
	v_pk_mul_f32 v[26:27], v[26:27], v[94:95]
	v_pk_mul_f32 v[22:23], v[22:23], v[146:147]
	v_pk_mul_f32 v[18:19], v[18:19], v[150:151]
	v_pk_mul_f32 v[28:29], v[28:29], v[88:89]
	v_pk_mul_f32 v[24:25], v[24:25], v[92:93]
	v_pk_mul_f32 v[20:21], v[20:21], v[144:145]
	v_pk_mul_f32 v[16:17], v[16:17], v[148:149]
	v_pk_mul_f32 v[14:15], v[14:15], v[90:91]
	v_pk_mul_f32 v[10:11], v[10:11], v[94:95]
	v_pk_mul_f32 v[6:7], v[6:7], v[146:147]
	v_pk_mul_f32 v[2:3], v[2:3], v[150:151]
	v_pk_mul_f32 v[12:13], v[12:13], v[88:89]
	v_pk_mul_f32 v[8:9], v[8:9], v[92:93]
	v_pk_mul_f32 v[4:5], v[4:5], v[144:145]
	v_pk_mul_f32 v[0:1], v[0:1], v[148:149]
	v_pk_mul_f32 v[78:79], v[78:79], v[90:91]
	v_pk_mul_f32 v[74:75], v[74:75], v[94:95]
	v_pk_mul_f32 v[70:71], v[70:71], v[146:147]
	v_pk_mul_f32 v[66:67], v[66:67], v[150:151]
	v_pk_mul_f32 v[76:77], v[76:77], v[88:89]
	v_pk_mul_f32 v[72:73], v[72:73], v[92:93]
	v_pk_mul_f32 v[68:69], v[68:69], v[144:145]
	v_pk_mul_f32 v[64:65], v[64:65], v[148:149]

.LBB0_1058:
	s_add_i32 s1, s40, 0xffffff78
	s_lshl_b32 s0, s38, 3
	s_max_i32 s1, s1, 0
	s_mulk_i32 s1, 0x48
	s_add_i32 s0, s42, s0
	s_add_i32 s43, s0, s1
	s_cmpk_gt_i32 s43, 0x47ff
	s_mov_b32 s1, 0
	s_cbranch_scc1 .LBB0_1135
	s_lshl_b32 s44, s40, 3
	s_add_u32 s45, s10, 0x17458000
	s_mul_i32 s0, s42, 0x2400
	s_addc_u32 s46, s11, 0
	s_add_i32 s0, s0, 0
	s_add_u32 s47, s10, 0x7458000
	s_addc_u32 s48, s11, 0
	s_add_u32 s49, s10, 0x6458000
	s_addc_u32 s50, s11, 0
	s_add_u32 s51, s10, 0x5458000
	s_addc_u32 s52, s11, 0
	s_add_u32 s53, s10, 0x4d58000
	s_addc_u32 s54, s11, 0
	s_add_u32 s55, s10, 0x158000
	s_addc_u32 s56, s11, 0
	s_add_u32 s57, s10, 0x3390c000
	s_addc_u32 s58, s11, 0
	s_add_u32 s59, s10, 0x35e0c000
	v_lshlrev_b32_e32 v2, 1, v86
	v_and_b32_e32 v0, 60, v0
	v_and_b32_e32 v80, 48, v54
	s_addc_u32 s60, s11, 0
	v_and_b32_e32 v2, 0x60, v2
	v_and_b32_e32 v8, 7, v85
	v_lshrrev_b32_e32 v90, 3, v86
	v_mov_b32_e32 v79, 0
	v_add_u32_e32 v1, s0, v76
	v_mul_u32_u24_e32 v3, 0x50, v0
	v_add_u32_e32 v4, s0, v80
	v_mul_u32_u24_e32 v5, 0x50, v87
	s_add_u32 s61, s10, 0x3760c000
	v_add_u32_e32 v6, s0, v2
	v_mul_u32_u24_e32 v7, 0x90, v0
	v_lshlrev_b32_e32 v2, 3, v8
	v_lshl_add_u32 v8, v8, 4, s0
	v_mul_u32_u24_e32 v9, 0x90, v90
	v_mov_b32_e32 v81, v79
	v_or_b32_e32 v77, 16, v87
	v_or_b32_e32 v88, 32, v87
	v_or_b32_e32 v89, 48, v87
	s_addc_u32 s62, s11, 0
	v_or_b32_e32 v91, 8, v90
	v_or_b32_e32 v92, 16, v90
	v_or_b32_e32 v93, 24, v90
	v_or_b32_e32 v94, 32, v90
	v_or_b32_e32 v95, 40, v90
	v_or_b32_e32 v96, 48, v90
	v_or_b32_e32 v97, 56, v90
	s_add_i32 s63, 0, 0x204f8
	s_movk_i32 s64, 0x2000
	s_movk_i32 s65, 0x4000
	s_movk_i32 s66, 0x6000
	s_mov_b32 s67, 0x12000
	s_mov_b32 s68, 0xc3e00000
	v_add_u32_e32 v98, v1, v3
	v_add_u32_e32 v99, v4, v5
	s_movk_i32 s69, 0x3000
	s_movk_i32 s70, 0x5000
	s_movk_i32 s71, 0x7000
	s_add_i32 s72, 0, 0x204c0
	s_add_i32 s73, 0, 0x204b8
	s_add_i32 s74, 0, 0x204b0
	s_add_i32 s75, 0, 0x204a8
	s_add_i32 s76, 0, 0x20458
	s_add_i32 s77, 0, 0x20448
	s_add_i32 s78, 0, 0x20440
	s_mov_b32 s79, 0x9000
	s_mov_b32 s80, 0x1b000
	s_mov_b32 s81, 0x25000
	s_mov_b32 s82, 0x2e000
	s_mov_b32 s83, 0x37000
	s_mov_b32 s84, 0x41000
	s_mov_b32 s85, 0x4a000
	s_mov_b32 s86, 0x53000
	s_mov_b32 s87, 0x5d000
	s_mov_b32 s88, 0x66000
	s_mov_b32 s89, 0x6f000
	s_mov_b32 s90, 0x79000
	s_mov_b32 s91, 0x82000
	s_mov_b32 s92, 0x8b000
	v_add_u32_e32 v100, v6, v7
	v_lshlrev_b32_e32 v78, 1, v2
	v_lshlrev_b32_e32 v82, 2, v0
	v_mov_b32_e32 v101, 0x43e00000
	v_mov_b32_e32 v104, v79
	v_mov_b32_e32 v105, v79
	v_mov_b32_e32 v106, v79
	v_mov_b32_e32 v107, v79
	v_add_u32_e32 v102, v8, v9
	s_branch .LBB0_1062

.LBB0_1061:
	s_add_i32 s43, s43, s44
	s_cmpk_lt_i32 s43, 0x4800
	s_cbranch_scc0 .LBB0_1134
